# P1 EpiProj epilogues: next accumulator group's row-ss word and rope row touched (dummy dword loads into dead VGPRs) before the current group's load wait, so its real loads hit L1; on top of v11
# speedup vs baseline: 1.0005x; 1.0005x over previous
;     __device__ __forceinline__ void operator()(const f32x4 (&acc)[2][2][4][2], const Unit& u, int wr, int wc, int fr, int fq) const {
;     ...
;                 const int rit = ai * HALF + wr * 64 + m * 16 + fr, s = (u.pm & 15) * 256 + rit, grow = u.pm * 256 + rit;
;                 const float rs = rsqrtf(ss[grow] * (1.0f / 4096.0f) + RMS_EPS) * sc;
;                 f32x4 c0 = {1.f, 1.f, 1.f, 1.f}, c1 = c0, s0 = {0.f, 0.f, 0.f, 0.f}, s1 = s0;
;                 if (rope) { const float* t = cs + (size_t)s * 32 + 8 * (fq & 1); c0 = *(const f32x4*)t; c1 = *(const f32x4*)(t + 4); s0 = *(const f32x4*)(t + 16); s1 = *(const f32x4*)(t + 20); }
; #pragma unroll
;                 for (int bj = 0; bj < 2; ++bj) {
;                     f32x4 v0 = acc[ai][bj][m][0] * rs, v1 = acc[ai][bj][m][1] * rs;
;                     if (rope) { rope4(v0, c0, s0, fq); rope4(v1, c1, s1, fq); }
.LBB0_179:
	v_add_u32_e32 v246, s71, v187
	v_ashrrev_i32_e32 v247, 31, v246
	v_lshl_add_u64 v[246:247], v[246:247], 2, s[20:21]
	global_load_dword v248, v[246:247], off
	v_add_u32_e32 v246, s72, v187
	v_ashrrev_i32_e32 v247, 31, v246
	v_lshlrev_b64 v[246:247], 7, v[246:247]
	v_lshl_add_u64 v[246:247], v[156:157], 0, v[246:247]
	global_load_dword v249, v[246:247], off
	global_load_dword v249, v[246:247], off offset:64
	s_waitcnt vmcnt(0)
	v_fmamk_f32 v170, v170, 0x39800000, v197
	v_mul_f32_e32 v171, 0x4b800000, v170
	v_cmp_gt_f32_e32 vcc, s68, v170
	s_nop 1
	v_cndmask_b32_e32 v170, v170, v171, vcc
	v_rsq_f32_e32 v170, v170
	s_nop 0
	v_mul_f32_e32 v171, 0x45800000, v170
	v_cndmask_b32_e32 v176, v170, v171, vcc
	v_pk_mul_f32 v[170:171], v[124:125], v[176:177] op_sel_hi:[1,0]
	v_cndmask_b32_e64 v124, 0, 1, s[40:41]
	v_pk_mul_f32 v[178:179], v[128:129], v[176:177] op_sel_hi:[1,0]
	v_pk_mul_f32 v[182:183], v[126:127], v[176:177] op_sel_hi:[1,0]
	v_cmp_ne_u32_e64 s[12:13], 1, v124
	s_andn2_b64 vcc, exec, s[40:41]
	v_pk_mul_f32 v[174:175], v[122:123], v[176:177] op_sel_hi:[1,0]
	s_cbranch_vccnz .LBB0_186
	s_cmp_lt_i32 s43, 5
	s_cbranch_scc1 .LBB0_182
	s_cmp_lg_u32 s43, 5
	s_cselect_b64 s[10:11], -1, 0
	s_cbranch_execz .LBB0_183
	s_branch .LBB0_184

;     __device__ __forceinline__ void operator()(const f32x4 (&acc)[2][2][4][2], const Unit& u, int wr, int wc, int fr, int fq) const {
;     ...
;                 const int rit = ai * HALF + wr * 64 + m * 16 + fr, s = (u.pm & 15) * 256 + rit, grow = u.pm * 256 + rit;
;                 const float rs = rsqrtf(ss[grow] * (1.0f / 4096.0f) + RMS_EPS) * sc;
;                 f32x4 c0 = {1.f, 1.f, 1.f, 1.f}, c1 = c0, s0 = {0.f, 0.f, 0.f, 0.f}, s1 = s0;
;                 if (rope) { const float* t = cs + (size_t)s * 32 + 8 * (fq & 1); c0 = *(const f32x4*)t; c1 = *(const f32x4*)(t + 4); s0 = *(const f32x4*)(t + 16); s1 = *(const f32x4*)(t + 20); }
; #pragma unroll
;                 for (int bj = 0; bj < 2; ++bj) {
;                     f32x4 v0 = acc[ai][bj][m][0] * rs, v1 = acc[ai][bj][m][1] * rs;
;                     if (rope) { rope4(v0, c0, s0, fq); rope4(v1, c1, s1, fq); }
.LBB0_217:
	v_add_u32_e32 v246, s71, v188
	v_ashrrev_i32_e32 v247, 31, v246
	v_lshl_add_u64 v[246:247], v[246:247], 2, s[20:21]
	global_load_dword v248, v[246:247], off
	v_add_u32_e32 v246, s72, v188
	v_ashrrev_i32_e32 v247, 31, v246
	v_lshlrev_b64 v[246:247], 7, v[246:247]
	v_lshl_add_u64 v[246:247], v[156:157], 0, v[246:247]
	global_load_dword v249, v[246:247], off
	global_load_dword v249, v[246:247], off offset:64
	s_waitcnt vmcnt(0)
	v_fmamk_f32 v130, v130, 0x39800000, v197
	v_mul_f32_e32 v131, 0x4b800000, v130
	v_cmp_gt_f32_e32 vcc, s68, v130
	s_nop 1
	v_cndmask_b32_e32 v130, v130, v131, vcc
	v_rsq_f32_e32 v130, v130
	s_nop 0
	v_mul_f32_e32 v131, 0x45800000, v130
	v_cndmask_b32_e32 v136, v130, v131, vcc
	v_pk_mul_f32 v[138:139], v[112:113], v[136:137] op_sel_hi:[1,0]
	v_pk_mul_f32 v[142:143], v[110:111], v[136:137] op_sel_hi:[1,0]
	v_pk_mul_f32 v[130:131], v[108:109], v[136:137] op_sel_hi:[1,0]
	s_and_b64 vcc, exec, s[12:13]
	v_pk_mul_f32 v[134:135], v[106:107], v[136:137] op_sel_hi:[1,0]
	s_cbranch_vccnz .LBB0_224
	s_cmp_lt_i32 s43, 5
	s_cbranch_scc1 .LBB0_220
	s_cmp_lg_u32 s43, 5
	s_cselect_b64 s[56:57], -1, 0
	s_cbranch_execz .LBB0_221
	s_branch .LBB0_222

;     __device__ __forceinline__ void operator()(const f32x4 (&acc)[2][2][4][2], const Unit& u, int wr, int wc, int fr, int fq) const {
;     ...
;                 const int rit = ai * HALF + wr * 64 + m * 16 + fr, s = (u.pm & 15) * 256 + rit, grow = u.pm * 256 + rit;
;                 const float rs = rsqrtf(ss[grow] * (1.0f / 4096.0f) + RMS_EPS) * sc;
;                 f32x4 c0 = {1.f, 1.f, 1.f, 1.f}, c1 = c0, s0 = {0.f, 0.f, 0.f, 0.f}, s1 = s0;
;                 if (rope) { const float* t = cs + (size_t)s * 32 + 8 * (fq & 1); c0 = *(const f32x4*)t; c1 = *(const f32x4*)(t + 4); s0 = *(const f32x4*)(t + 16); s1 = *(const f32x4*)(t + 20); }
; #pragma unroll
;                 for (int bj = 0; bj < 2; ++bj) {
;                     f32x4 v0 = acc[ai][bj][m][0] * rs, v1 = acc[ai][bj][m][1] * rs;
;                     if (rope) { rope4(v0, c0, s0, fq); rope4(v1, c1, s1, fq); }
.LBB0_255:
	v_add_u32_e32 v246, s71, v189
	v_ashrrev_i32_e32 v247, 31, v246
	v_lshl_add_u64 v[246:247], v[246:247], 2, s[20:21]
	global_load_dword v248, v[246:247], off
	v_add_u32_e32 v246, s72, v189
	v_ashrrev_i32_e32 v247, 31, v246
	v_lshlrev_b64 v[246:247], 7, v[246:247]
	v_lshl_add_u64 v[246:247], v[156:157], 0, v[246:247]
	global_load_dword v249, v[246:247], off
	global_load_dword v249, v[246:247], off offset:64
	s_waitcnt vmcnt(0)
	v_fmamk_f32 v114, v114, 0x39800000, v197
	v_mul_f32_e32 v115, 0x4b800000, v114
	v_cmp_gt_f32_e32 vcc, s68, v114
	s_nop 1
	v_cndmask_b32_e32 v114, v114, v115, vcc
	v_rsq_f32_e32 v114, v114
	s_nop 0
	v_mul_f32_e32 v115, 0x45800000, v114
	v_cndmask_b32_e32 v120, v114, v115, vcc
	v_pk_mul_f32 v[122:123], v[96:97], v[120:121] op_sel_hi:[1,0]
	v_pk_mul_f32 v[126:127], v[94:95], v[120:121] op_sel_hi:[1,0]
	v_pk_mul_f32 v[114:115], v[92:93], v[120:121] op_sel_hi:[1,0]
	s_and_b64 vcc, exec, s[12:13]
	v_pk_mul_f32 v[118:119], v[90:91], v[120:121] op_sel_hi:[1,0]
	s_cbranch_vccnz .LBB0_262
	s_cmp_lt_i32 s43, 5
	s_cbranch_scc1 .LBB0_258
	s_cmp_lg_u32 s43, 5
	s_cselect_b64 s[56:57], -1, 0
	s_cbranch_execz .LBB0_259
	s_branch .LBB0_260

;     __device__ __forceinline__ void operator()(const f32x4 (&acc)[2][2][4][2], const Unit& u, int wr, int wc, int fr, int fq) const {
;     ...
;                 const int rit = ai * HALF + wr * 64 + m * 16 + fr, s = (u.pm & 15) * 256 + rit, grow = u.pm * 256 + rit;
;                 const float rs = rsqrtf(ss[grow] * (1.0f / 4096.0f) + RMS_EPS) * sc;
;                 f32x4 c0 = {1.f, 1.f, 1.f, 1.f}, c1 = c0, s0 = {0.f, 0.f, 0.f, 0.f}, s1 = s0;
;                 if (rope) { const float* t = cs + (size_t)s * 32 + 8 * (fq & 1); c0 = *(const f32x4*)t; c1 = *(const f32x4*)(t + 4); s0 = *(const f32x4*)(t + 16); s1 = *(const f32x4*)(t + 20); }
; #pragma unroll
;                 for (int bj = 0; bj < 2; ++bj) {
;                     f32x4 v0 = acc[ai][bj][m][0] * rs, v1 = acc[ai][bj][m][1] * rs;
;                     if (rope) { rope4(v0, c0, s0, fq); rope4(v1, c1, s1, fq); }
.LBB0_293:
	v_add_u32_e32 v246, s71, v190
	v_ashrrev_i32_e32 v247, 31, v246
	v_lshl_add_u64 v[246:247], v[246:247], 2, s[20:21]
	global_load_dword v248, v[246:247], off
	v_add_u32_e32 v246, s72, v190
	v_ashrrev_i32_e32 v247, 31, v246
	v_lshlrev_b64 v[246:247], 7, v[246:247]
	v_lshl_add_u64 v[246:247], v[156:157], 0, v[246:247]
	global_load_dword v249, v[246:247], off
	global_load_dword v249, v[246:247], off offset:64
	s_waitcnt vmcnt(0)
	v_fmamk_f32 v98, v98, 0x39800000, v197
	v_mul_f32_e32 v99, 0x4b800000, v98
	v_cmp_gt_f32_e32 vcc, s68, v98
	s_nop 1
	v_cndmask_b32_e32 v98, v98, v99, vcc
	v_rsq_f32_e32 v98, v98
	s_nop 0
	v_mul_f32_e32 v99, 0x45800000, v98
	v_cndmask_b32_e32 v104, v98, v99, vcc
	v_pk_mul_f32 v[106:107], v[80:81], v[104:105] op_sel_hi:[1,0]
	v_pk_mul_f32 v[110:111], v[78:79], v[104:105] op_sel_hi:[1,0]
	v_pk_mul_f32 v[98:99], v[76:77], v[104:105] op_sel_hi:[1,0]
	s_and_b64 vcc, exec, s[12:13]
	v_pk_mul_f32 v[102:103], v[74:75], v[104:105] op_sel_hi:[1,0]
	s_cbranch_vccnz .LBB0_300
	s_cmp_lt_i32 s43, 5
	s_cbranch_scc1 .LBB0_296
	s_cmp_lg_u32 s43, 5
	s_cselect_b64 s[56:57], -1, 0
	s_cbranch_execz .LBB0_297
	s_branch .LBB0_298

;     __device__ __forceinline__ void operator()(const f32x4 (&acc)[2][2][4][2], const Unit& u, int wr, int wc, int fr, int fq) const {
;     ...
;                 const int rit = ai * HALF + wr * 64 + m * 16 + fr, s = (u.pm & 15) * 256 + rit, grow = u.pm * 256 + rit;
;                 const float rs = rsqrtf(ss[grow] * (1.0f / 4096.0f) + RMS_EPS) * sc;
;                 f32x4 c0 = {1.f, 1.f, 1.f, 1.f}, c1 = c0, s0 = {0.f, 0.f, 0.f, 0.f}, s1 = s0;
;                 if (rope) { const float* t = cs + (size_t)s * 32 + 8 * (fq & 1); c0 = *(const f32x4*)t; c1 = *(const f32x4*)(t + 4); s0 = *(const f32x4*)(t + 16); s1 = *(const f32x4*)(t + 20); }
; #pragma unroll
;                 for (int bj = 0; bj < 2; ++bj) {
;                     f32x4 v0 = acc[ai][bj][m][0] * rs, v1 = acc[ai][bj][m][1] * rs;
;                     if (rope) { rope4(v0, c0, s0, fq); rope4(v1, c1, s1, fq); }
.LBB0_331:
	v_add_u32_e32 v246, s71, v191
	v_ashrrev_i32_e32 v247, 31, v246
	v_lshl_add_u64 v[246:247], v[246:247], 2, s[20:21]
	global_load_dword v248, v[246:247], off
	v_add_u32_e32 v246, s72, v191
	v_ashrrev_i32_e32 v247, 31, v246
	v_lshlrev_b64 v[246:247], 7, v[246:247]
	v_lshl_add_u64 v[246:247], v[156:157], 0, v[246:247]
	global_load_dword v249, v[246:247], off
	global_load_dword v249, v[246:247], off offset:64
	s_waitcnt vmcnt(0)
	v_fmamk_f32 v82, v82, 0x39800000, v197
	v_mul_f32_e32 v83, 0x4b800000, v82
	v_cmp_gt_f32_e32 vcc, s68, v82
	s_nop 1
	v_cndmask_b32_e32 v82, v82, v83, vcc
	v_rsq_f32_e32 v82, v82
	s_nop 0
	v_mul_f32_e32 v83, 0x45800000, v82
	v_cndmask_b32_e32 v88, v82, v83, vcc
	v_pk_mul_f32 v[90:91], v[64:65], v[88:89] op_sel_hi:[1,0]
	v_pk_mul_f32 v[94:95], v[62:63], v[88:89] op_sel_hi:[1,0]
	v_pk_mul_f32 v[82:83], v[60:61], v[88:89] op_sel_hi:[1,0]
	s_and_b64 vcc, exec, s[12:13]
	v_pk_mul_f32 v[86:87], v[58:59], v[88:89] op_sel_hi:[1,0]
	s_cbranch_vccnz .LBB0_338
	s_cmp_lt_i32 s43, 5
	s_cbranch_scc1 .LBB0_334
	s_cmp_lg_u32 s43, 5
	s_cselect_b64 s[56:57], -1, 0
	s_cbranch_execz .LBB0_335
	s_branch .LBB0_336

;     __device__ __forceinline__ void operator()(const f32x4 (&acc)[2][2][4][2], const Unit& u, int wr, int wc, int fr, int fq) const {
;     ...
;                 const int rit = ai * HALF + wr * 64 + m * 16 + fr, s = (u.pm & 15) * 256 + rit, grow = u.pm * 256 + rit;
;                 const float rs = rsqrtf(ss[grow] * (1.0f / 4096.0f) + RMS_EPS) * sc;
;                 f32x4 c0 = {1.f, 1.f, 1.f, 1.f}, c1 = c0, s0 = {0.f, 0.f, 0.f, 0.f}, s1 = s0;
;                 if (rope) { const float* t = cs + (size_t)s * 32 + 8 * (fq & 1); c0 = *(const f32x4*)t; c1 = *(const f32x4*)(t + 4); s0 = *(const f32x4*)(t + 16); s1 = *(const f32x4*)(t + 20); }
; #pragma unroll
;                 for (int bj = 0; bj < 2; ++bj) {
;                     f32x4 v0 = acc[ai][bj][m][0] * rs, v1 = acc[ai][bj][m][1] * rs;
;                     if (rope) { rope4(v0, c0, s0, fq); rope4(v1, c1, s1, fq); }
.LBB0_369:
	v_add_u32_e32 v246, s71, v192
	v_ashrrev_i32_e32 v247, 31, v246
	v_lshl_add_u64 v[246:247], v[246:247], 2, s[20:21]
	global_load_dword v248, v[246:247], off
	v_add_u32_e32 v246, s72, v192
	v_ashrrev_i32_e32 v247, 31, v246
	v_lshlrev_b64 v[246:247], 7, v[246:247]
	v_lshl_add_u64 v[246:247], v[156:157], 0, v[246:247]
	global_load_dword v249, v[246:247], off
	global_load_dword v249, v[246:247], off offset:64
	s_waitcnt vmcnt(0)
	v_fmamk_f32 v66, v66, 0x39800000, v197
	v_mul_f32_e32 v67, 0x4b800000, v66
	v_cmp_gt_f32_e32 vcc, s68, v66
	s_nop 1
	v_cndmask_b32_e32 v66, v66, v67, vcc
	v_rsq_f32_e32 v66, v66
	s_nop 0
	v_mul_f32_e32 v67, 0x45800000, v66
	v_cndmask_b32_e32 v72, v66, v67, vcc
	v_pk_mul_f32 v[74:75], v[48:49], v[72:73] op_sel_hi:[1,0]
	v_pk_mul_f32 v[78:79], v[46:47], v[72:73] op_sel_hi:[1,0]
	v_pk_mul_f32 v[66:67], v[44:45], v[72:73] op_sel_hi:[1,0]
	s_and_b64 vcc, exec, s[12:13]
	v_pk_mul_f32 v[70:71], v[42:43], v[72:73] op_sel_hi:[1,0]
	s_cbranch_vccnz .LBB0_376
	s_cmp_lt_i32 s43, 5
	s_cbranch_scc1 .LBB0_372
	s_cmp_lg_u32 s43, 5
	s_cselect_b64 s[56:57], -1, 0
	s_cbranch_execz .LBB0_373
	s_branch .LBB0_374

;     __device__ __forceinline__ void operator()(const f32x4 (&acc)[2][2][4][2], const Unit& u, int wr, int wc, int fr, int fq) const {
;     ...
;                 const int rit = ai * HALF + wr * 64 + m * 16 + fr, s = (u.pm & 15) * 256 + rit, grow = u.pm * 256 + rit;
;                 const float rs = rsqrtf(ss[grow] * (1.0f / 4096.0f) + RMS_EPS) * sc;
;                 f32x4 c0 = {1.f, 1.f, 1.f, 1.f}, c1 = c0, s0 = {0.f, 0.f, 0.f, 0.f}, s1 = s0;
;                 if (rope) { const float* t = cs + (size_t)s * 32 + 8 * (fq & 1); c0 = *(const f32x4*)t; c1 = *(const f32x4*)(t + 4); s0 = *(const f32x4*)(t + 16); s1 = *(const f32x4*)(t + 20); }
; #pragma unroll
;                 for (int bj = 0; bj < 2; ++bj) {
;                     f32x4 v0 = acc[ai][bj][m][0] * rs, v1 = acc[ai][bj][m][1] * rs;
;                     if (rope) { rope4(v0, c0, s0, fq); rope4(v1, c1, s1, fq); }
.LBB0_407:
	v_add_u32_e32 v246, s71, v193
	v_ashrrev_i32_e32 v247, 31, v246
	v_lshl_add_u64 v[246:247], v[246:247], 2, s[20:21]
	global_load_dword v248, v[246:247], off
	v_add_u32_e32 v246, s72, v193
	v_ashrrev_i32_e32 v247, 31, v246
	v_lshlrev_b64 v[246:247], 7, v[246:247]
	v_lshl_add_u64 v[246:247], v[156:157], 0, v[246:247]
	global_load_dword v249, v[246:247], off
	global_load_dword v249, v[246:247], off offset:64
	s_waitcnt vmcnt(0)
	v_fmamk_f32 v50, v50, 0x39800000, v197
	v_mul_f32_e32 v51, 0x4b800000, v50
	v_cmp_gt_f32_e32 vcc, s68, v50
	s_nop 1
	v_cndmask_b32_e32 v50, v50, v51, vcc
	v_rsq_f32_e32 v50, v50
	s_nop 0
	v_mul_f32_e32 v51, 0x45800000, v50
	v_cndmask_b32_e32 v56, v50, v51, vcc
	v_pk_mul_f32 v[58:59], v[32:33], v[56:57] op_sel_hi:[1,0]
	v_pk_mul_f32 v[62:63], v[30:31], v[56:57] op_sel_hi:[1,0]
	v_pk_mul_f32 v[50:51], v[28:29], v[56:57] op_sel_hi:[1,0]
	s_and_b64 vcc, exec, s[12:13]
	v_pk_mul_f32 v[54:55], v[26:27], v[56:57] op_sel_hi:[1,0]
	s_cbranch_vccnz .LBB0_414
	s_cmp_lt_i32 s43, 5
	s_cbranch_scc1 .LBB0_410
	s_cmp_lg_u32 s43, 5
	s_cselect_b64 s[56:57], -1, 0
	s_cbranch_execz .LBB0_411
	s_branch .LBB0_412

;     __device__ __forceinline__ void operator()(const f32x4 (&acc)[2][2][4][2], const Unit& u, int wr, int wc, int fr, int fq) const {
;     ...
;                 const int rit = ai * HALF + wr * 64 + m * 16 + fr, s = (u.pm & 15) * 256 + rit, grow = u.pm * 256 + rit;
;                 const float rs = rsqrtf(ss[grow] * (1.0f / 4096.0f) + RMS_EPS) * sc;
;                 f32x4 c0 = {1.f, 1.f, 1.f, 1.f}, c1 = c0, s0 = {0.f, 0.f, 0.f, 0.f}, s1 = s0;
;                 if (rope) { const float* t = cs + (size_t)s * 32 + 8 * (fq & 1); c0 = *(const f32x4*)t; c1 = *(const f32x4*)(t + 4); s0 = *(const f32x4*)(t + 16); s1 = *(const f32x4*)(t + 20); }
; #pragma unroll
;                 for (int bj = 0; bj < 2; ++bj) {
;                     f32x4 v0 = acc[ai][bj][m][0] * rs, v1 = acc[ai][bj][m][1] * rs;
;                     if (rope) { rope4(v0, c0, s0, fq); rope4(v1, c1, s1, fq); }
.LBB0_545:
	v_add_u32_e32 v246, s69, v195
	v_ashrrev_i32_e32 v247, 31, v246
	v_lshl_add_u64 v[246:247], v[246:247], 2, s[20:21]
	global_load_dword v248, v[246:247], off
	v_add_u32_e32 v246, s70, v195
	v_ashrrev_i32_e32 v247, 31, v246
	v_lshlrev_b64 v[246:247], 7, v[246:247]
	v_lshl_add_u64 v[246:247], v[172:173], 0, v[246:247]
	global_load_dword v249, v[246:247], off
	global_load_dword v249, v[246:247], off offset:64
	s_waitcnt vmcnt(0)
	v_fmamk_f32 v18, v18, 0x39800000, v205
	v_mul_f32_e32 v19, 0x4b800000, v18
	v_cmp_gt_f32_e32 vcc, s66, v18
	v_cndmask_b32_e64 v21, 0, 1, s[38:39]
	v_cmp_ne_u32_e64 s[10:11], 1, v21
	v_cndmask_b32_e32 v18, v18, v19, vcc
	v_rsq_f32_e32 v18, v18
	s_nop 0
	v_mul_f32_e32 v19, 0x45800000, v18
	v_cndmask_b32_e32 v18, v18, v19, vcc
	v_mul_f32_e32 v24, 0x3c800000, v18
	v_pk_mul_f32 v[26:27], v[160:161], v[24:25] op_sel_hi:[1,0]
	v_pk_mul_f32 v[30:31], v[158:159], v[24:25] op_sel_hi:[1,0]
	v_pk_mul_f32 v[18:19], v[156:157], v[24:25] op_sel_hi:[1,0]
	s_andn2_b64 vcc, exec, s[38:39]
	v_pk_mul_f32 v[22:23], v[154:155], v[24:25] op_sel_hi:[1,0]
	s_cbranch_vccnz .LBB0_552
	s_cmp_lt_i32 s3, 2
	s_cbranch_scc1 .LBB0_548
	s_cmp_lg_u32 s3, 2
	s_cselect_b64 s[8:9], -1, 0
	s_cbranch_execz .LBB0_549
	s_branch .LBB0_550

;     __device__ __forceinline__ void operator()(const f32x4 (&acc)[2][2][4][2], const Unit& u, int wr, int wc, int fr, int fq) const {
;     ...
;                 const int rit = ai * HALF + wr * 64 + m * 16 + fr, s = (u.pm & 15) * 256 + rit, grow = u.pm * 256 + rit;
;                 const float rs = rsqrtf(ss[grow] * (1.0f / 4096.0f) + RMS_EPS) * sc;
;                 f32x4 c0 = {1.f, 1.f, 1.f, 1.f}, c1 = c0, s0 = {0.f, 0.f, 0.f, 0.f}, s1 = s0;
;                 if (rope) { const float* t = cs + (size_t)s * 32 + 8 * (fq & 1); c0 = *(const f32x4*)t; c1 = *(const f32x4*)(t + 4); s0 = *(const f32x4*)(t + 16); s1 = *(const f32x4*)(t + 20); }
; #pragma unroll
;                 for (int bj = 0; bj < 2; ++bj) {
;                     f32x4 v0 = acc[ai][bj][m][0] * rs, v1 = acc[ai][bj][m][1] * rs;
;                     if (rope) { rope4(v0, c0, s0, fq); rope4(v1, c1, s1, fq); }
.LBB0_583:
	v_add_u32_e32 v246, s69, v196
	v_ashrrev_i32_e32 v247, 31, v246
	v_lshl_add_u64 v[246:247], v[246:247], 2, s[20:21]
	global_load_dword v248, v[246:247], off
	v_add_u32_e32 v246, s70, v196
	v_ashrrev_i32_e32 v247, 31, v246
	v_lshlrev_b64 v[246:247], 7, v[246:247]
	v_lshl_add_u64 v[246:247], v[172:173], 0, v[246:247]
	global_load_dword v249, v[246:247], off
	global_load_dword v249, v[246:247], off offset:64
	s_waitcnt vmcnt(0)
	v_fmamk_f32 v147, v148, 0x39800000, v205
	v_mul_f32_e32 v148, 0x4b800000, v147
	v_cmp_gt_f32_e32 vcc, s66, v147
	s_nop 1
	v_cndmask_b32_e32 v147, v147, v148, vcc
	v_rsq_f32_e32 v147, v147
	s_nop 0
	v_mul_f32_e32 v148, 0x45800000, v147
	v_cndmask_b32_e32 v147, v147, v148, vcc
	v_mul_f32_e32 v148, 0x3c800000, v147
	v_pk_mul_f32 v[144:145], v[144:145], v[148:149] op_sel_hi:[1,0]
	v_pk_mul_f32 v[142:143], v[142:143], v[148:149] op_sel_hi:[1,0]
	v_pk_mul_f32 v[140:141], v[140:141], v[148:149] op_sel_hi:[1,0]
	s_and_b64 vcc, exec, s[10:11]
	v_pk_mul_f32 v[138:139], v[138:139], v[148:149] op_sel_hi:[1,0]
	s_cbranch_vccnz .LBB0_590
	s_cmp_lt_i32 s3, 2
	s_cbranch_scc1 .LBB0_586
	s_cmp_lg_u32 s3, 2
	s_cselect_b64 s[52:53], -1, 0
	s_cbranch_execz .LBB0_587
	s_branch .LBB0_588

;     __device__ __forceinline__ void operator()(const f32x4 (&acc)[2][2][4][2], const Unit& u, int wr, int wc, int fr, int fq) const {
;     ...
;                 const int rit = ai * HALF + wr * 64 + m * 16 + fr, s = (u.pm & 15) * 256 + rit, grow = u.pm * 256 + rit;
;                 const float rs = rsqrtf(ss[grow] * (1.0f / 4096.0f) + RMS_EPS) * sc;
;                 f32x4 c0 = {1.f, 1.f, 1.f, 1.f}, c1 = c0, s0 = {0.f, 0.f, 0.f, 0.f}, s1 = s0;
;                 if (rope) { const float* t = cs + (size_t)s * 32 + 8 * (fq & 1); c0 = *(const f32x4*)t; c1 = *(const f32x4*)(t + 4); s0 = *(const f32x4*)(t + 16); s1 = *(const f32x4*)(t + 20); }
; #pragma unroll
;                 for (int bj = 0; bj < 2; ++bj) {
;                     f32x4 v0 = acc[ai][bj][m][0] * rs, v1 = acc[ai][bj][m][1] * rs;
;                     if (rope) { rope4(v0, c0, s0, fq); rope4(v1, c1, s1, fq); }
.LBB0_621:
	v_add_u32_e32 v246, s69, v197
	v_ashrrev_i32_e32 v247, 31, v246
	v_lshl_add_u64 v[246:247], v[246:247], 2, s[20:21]
	global_load_dword v248, v[246:247], off
	v_add_u32_e32 v246, s70, v197
	v_ashrrev_i32_e32 v247, 31, v246
	v_lshlrev_b64 v[246:247], 7, v[246:247]
	v_lshl_add_u64 v[246:247], v[172:173], 0, v[246:247]
	global_load_dword v249, v[246:247], off
	global_load_dword v249, v[246:247], off offset:64
	s_waitcnt vmcnt(0)
	v_fmamk_f32 v147, v148, 0x39800000, v205
	v_mul_f32_e32 v148, 0x4b800000, v147
	v_cmp_gt_f32_e32 vcc, s66, v147
	s_nop 1
	v_cndmask_b32_e32 v147, v147, v148, vcc
	v_rsq_f32_e32 v147, v147
	s_nop 0
	v_mul_f32_e32 v148, 0x45800000, v147
	v_cndmask_b32_e32 v147, v147, v148, vcc
	v_mul_f32_e32 v148, 0x3c800000, v147
	v_pk_mul_f32 v[128:129], v[128:129], v[148:149] op_sel_hi:[1,0]
	v_pk_mul_f32 v[126:127], v[126:127], v[148:149] op_sel_hi:[1,0]
	v_pk_mul_f32 v[124:125], v[124:125], v[148:149] op_sel_hi:[1,0]
	s_and_b64 vcc, exec, s[10:11]
	v_pk_mul_f32 v[122:123], v[122:123], v[148:149] op_sel_hi:[1,0]
	s_cbranch_vccnz .LBB0_628
	s_cmp_lt_i32 s3, 2
	s_cbranch_scc1 .LBB0_624
	s_cmp_lg_u32 s3, 2
	s_cselect_b64 s[52:53], -1, 0
	s_cbranch_execz .LBB0_625
	s_branch .LBB0_626

;     __device__ __forceinline__ void operator()(const f32x4 (&acc)[2][2][4][2], const Unit& u, int wr, int wc, int fr, int fq) const {
;     ...
;                 const int rit = ai * HALF + wr * 64 + m * 16 + fr, s = (u.pm & 15) * 256 + rit, grow = u.pm * 256 + rit;
;                 const float rs = rsqrtf(ss[grow] * (1.0f / 4096.0f) + RMS_EPS) * sc;
;                 f32x4 c0 = {1.f, 1.f, 1.f, 1.f}, c1 = c0, s0 = {0.f, 0.f, 0.f, 0.f}, s1 = s0;
;                 if (rope) { const float* t = cs + (size_t)s * 32 + 8 * (fq & 1); c0 = *(const f32x4*)t; c1 = *(const f32x4*)(t + 4); s0 = *(const f32x4*)(t + 16); s1 = *(const f32x4*)(t + 20); }
; #pragma unroll
;                 for (int bj = 0; bj < 2; ++bj) {
;                     f32x4 v0 = acc[ai][bj][m][0] * rs, v1 = acc[ai][bj][m][1] * rs;
;                     if (rope) { rope4(v0, c0, s0, fq); rope4(v1, c1, s1, fq); }
.LBB0_659:
	v_add_u32_e32 v246, s69, v198
	v_ashrrev_i32_e32 v247, 31, v246
	v_lshl_add_u64 v[246:247], v[246:247], 2, s[20:21]
	global_load_dword v248, v[246:247], off
	v_add_u32_e32 v246, s70, v198
	v_ashrrev_i32_e32 v247, 31, v246
	v_lshlrev_b64 v[246:247], 7, v[246:247]
	v_lshl_add_u64 v[246:247], v[172:173], 0, v[246:247]
	global_load_dword v249, v[246:247], off
	global_load_dword v249, v[246:247], off offset:64
	s_waitcnt vmcnt(0)
	v_fmamk_f32 v147, v148, 0x39800000, v205
	v_mul_f32_e32 v148, 0x4b800000, v147
	v_cmp_gt_f32_e32 vcc, s66, v147
	s_nop 1
	v_cndmask_b32_e32 v147, v147, v148, vcc
	v_rsq_f32_e32 v147, v147
	s_nop 0
	v_mul_f32_e32 v148, 0x45800000, v147
	v_cndmask_b32_e32 v147, v147, v148, vcc
	v_mul_f32_e32 v148, 0x3c800000, v147
	v_pk_mul_f32 v[112:113], v[112:113], v[148:149] op_sel_hi:[1,0]
	v_pk_mul_f32 v[110:111], v[110:111], v[148:149] op_sel_hi:[1,0]
	v_pk_mul_f32 v[108:109], v[108:109], v[148:149] op_sel_hi:[1,0]
	s_and_b64 vcc, exec, s[10:11]
	v_pk_mul_f32 v[106:107], v[106:107], v[148:149] op_sel_hi:[1,0]
	s_cbranch_vccnz .LBB0_666
	s_cmp_lt_i32 s3, 2
	s_cbranch_scc1 .LBB0_662
	s_cmp_lg_u32 s3, 2
	s_cselect_b64 s[52:53], -1, 0
	s_cbranch_execz .LBB0_663
	s_branch .LBB0_664

;     __device__ __forceinline__ void operator()(const f32x4 (&acc)[2][2][4][2], const Unit& u, int wr, int wc, int fr, int fq) const {
;     ...
;                 const int rit = ai * HALF + wr * 64 + m * 16 + fr, s = (u.pm & 15) * 256 + rit, grow = u.pm * 256 + rit;
;                 const float rs = rsqrtf(ss[grow] * (1.0f / 4096.0f) + RMS_EPS) * sc;
;                 f32x4 c0 = {1.f, 1.f, 1.f, 1.f}, c1 = c0, s0 = {0.f, 0.f, 0.f, 0.f}, s1 = s0;
;                 if (rope) { const float* t = cs + (size_t)s * 32 + 8 * (fq & 1); c0 = *(const f32x4*)t; c1 = *(const f32x4*)(t + 4); s0 = *(const f32x4*)(t + 16); s1 = *(const f32x4*)(t + 20); }
; #pragma unroll
;                 for (int bj = 0; bj < 2; ++bj) {
;                     f32x4 v0 = acc[ai][bj][m][0] * rs, v1 = acc[ai][bj][m][1] * rs;
;                     if (rope) { rope4(v0, c0, s0, fq); rope4(v1, c1, s1, fq); }
.LBB0_697:
	v_add_u32_e32 v246, s69, v199
	v_ashrrev_i32_e32 v247, 31, v246
	v_lshl_add_u64 v[246:247], v[246:247], 2, s[20:21]
	global_load_dword v248, v[246:247], off
	v_add_u32_e32 v246, s70, v199
	v_ashrrev_i32_e32 v247, 31, v246
	v_lshlrev_b64 v[246:247], 7, v[246:247]
	v_lshl_add_u64 v[246:247], v[172:173], 0, v[246:247]
	global_load_dword v249, v[246:247], off
	global_load_dword v249, v[246:247], off offset:64
	s_waitcnt vmcnt(0)
	v_fmamk_f32 v147, v148, 0x39800000, v205
	v_mul_f32_e32 v148, 0x4b800000, v147
	v_cmp_gt_f32_e32 vcc, s66, v147
	s_nop 1
	v_cndmask_b32_e32 v147, v147, v148, vcc
	v_rsq_f32_e32 v147, v147
	s_nop 0
	v_mul_f32_e32 v148, 0x45800000, v147
	v_cndmask_b32_e32 v147, v147, v148, vcc
	v_mul_f32_e32 v148, 0x3c800000, v147
	v_pk_mul_f32 v[96:97], v[96:97], v[148:149] op_sel_hi:[1,0]
	v_pk_mul_f32 v[94:95], v[94:95], v[148:149] op_sel_hi:[1,0]
	v_pk_mul_f32 v[92:93], v[92:93], v[148:149] op_sel_hi:[1,0]
	s_and_b64 vcc, exec, s[10:11]
	v_pk_mul_f32 v[90:91], v[90:91], v[148:149] op_sel_hi:[1,0]
	s_cbranch_vccnz .LBB0_704
	s_cmp_lt_i32 s3, 2
	s_cbranch_scc1 .LBB0_700
	s_cmp_lg_u32 s3, 2
	s_cselect_b64 s[52:53], -1, 0
	s_cbranch_execz .LBB0_701
	s_branch .LBB0_702

;     __device__ __forceinline__ void operator()(const f32x4 (&acc)[2][2][4][2], const Unit& u, int wr, int wc, int fr, int fq) const {
;     ...
;                 const int rit = ai * HALF + wr * 64 + m * 16 + fr, s = (u.pm & 15) * 256 + rit, grow = u.pm * 256 + rit;
;                 const float rs = rsqrtf(ss[grow] * (1.0f / 4096.0f) + RMS_EPS) * sc;
;                 f32x4 c0 = {1.f, 1.f, 1.f, 1.f}, c1 = c0, s0 = {0.f, 0.f, 0.f, 0.f}, s1 = s0;
;                 if (rope) { const float* t = cs + (size_t)s * 32 + 8 * (fq & 1); c0 = *(const f32x4*)t; c1 = *(const f32x4*)(t + 4); s0 = *(const f32x4*)(t + 16); s1 = *(const f32x4*)(t + 20); }
; #pragma unroll
;                 for (int bj = 0; bj < 2; ++bj) {
;                     f32x4 v0 = acc[ai][bj][m][0] * rs, v1 = acc[ai][bj][m][1] * rs;
;                     if (rope) { rope4(v0, c0, s0, fq); rope4(v1, c1, s1, fq); }
.LBB0_735:
	v_add_u32_e32 v246, s69, v200
	v_ashrrev_i32_e32 v247, 31, v246
	v_lshl_add_u64 v[246:247], v[246:247], 2, s[20:21]
	global_load_dword v248, v[246:247], off
	v_add_u32_e32 v246, s70, v200
	v_ashrrev_i32_e32 v247, 31, v246
	v_lshlrev_b64 v[246:247], 7, v[246:247]
	v_lshl_add_u64 v[246:247], v[172:173], 0, v[246:247]
	global_load_dword v249, v[246:247], off
	global_load_dword v249, v[246:247], off offset:64
	s_waitcnt vmcnt(0)
	v_fmamk_f32 v147, v148, 0x39800000, v205
	v_mul_f32_e32 v148, 0x4b800000, v147
	v_cmp_gt_f32_e32 vcc, s66, v147
	s_nop 1
	v_cndmask_b32_e32 v147, v147, v148, vcc
	v_rsq_f32_e32 v147, v147
	s_nop 0
	v_mul_f32_e32 v148, 0x45800000, v147
	v_cndmask_b32_e32 v147, v147, v148, vcc
	v_mul_f32_e32 v148, 0x3c800000, v147
	v_pk_mul_f32 v[80:81], v[80:81], v[148:149] op_sel_hi:[1,0]
	v_pk_mul_f32 v[78:79], v[78:79], v[148:149] op_sel_hi:[1,0]
	v_pk_mul_f32 v[76:77], v[76:77], v[148:149] op_sel_hi:[1,0]
	s_and_b64 vcc, exec, s[10:11]
	v_pk_mul_f32 v[74:75], v[74:75], v[148:149] op_sel_hi:[1,0]
	s_cbranch_vccnz .LBB0_742
	s_cmp_lt_i32 s3, 2
	s_cbranch_scc1 .LBB0_738
	s_cmp_lg_u32 s3, 2
	s_cselect_b64 s[52:53], -1, 0
	s_cbranch_execz .LBB0_739
	s_branch .LBB0_740

;     __device__ __forceinline__ void operator()(const f32x4 (&acc)[2][2][4][2], const Unit& u, int wr, int wc, int fr, int fq) const {
;     ...
;                 const int rit = ai * HALF + wr * 64 + m * 16 + fr, s = (u.pm & 15) * 256 + rit, grow = u.pm * 256 + rit;
;                 const float rs = rsqrtf(ss[grow] * (1.0f / 4096.0f) + RMS_EPS) * sc;
;                 f32x4 c0 = {1.f, 1.f, 1.f, 1.f}, c1 = c0, s0 = {0.f, 0.f, 0.f, 0.f}, s1 = s0;
;                 if (rope) { const float* t = cs + (size_t)s * 32 + 8 * (fq & 1); c0 = *(const f32x4*)t; c1 = *(const f32x4*)(t + 4); s0 = *(const f32x4*)(t + 16); s1 = *(const f32x4*)(t + 20); }
; #pragma unroll
;                 for (int bj = 0; bj < 2; ++bj) {
;                     f32x4 v0 = acc[ai][bj][m][0] * rs, v1 = acc[ai][bj][m][1] * rs;
.LBB0_773:
	v_add_u32_e32 v246, s69, v201
	v_ashrrev_i32_e32 v247, 31, v246
	v_lshl_add_u64 v[246:247], v[246:247], 2, s[20:21]
	global_load_dword v248, v[246:247], off
	v_add_u32_e32 v246, s70, v201
	v_ashrrev_i32_e32 v247, 31, v246
	v_lshlrev_b64 v[246:247], 7, v[246:247]
	v_lshl_add_u64 v[246:247], v[172:173], 0, v[246:247]
	global_load_dword v249, v[246:247], off
	global_load_dword v249, v[246:247], off offset:64
	s_waitcnt vmcnt(0)
	v_fmamk_f32 v147, v148, 0x39800000, v205
	v_mul_f32_e32 v148, 0x4b800000, v147
	v_cmp_gt_f32_e32 vcc, s66, v147
	s_nop 1
	v_cndmask_b32_e32 v147, v147, v148, vcc
	v_rsq_f32_e32 v147, v147
	s_nop 0
	v_mul_f32_e32 v148, 0x45800000, v147
	v_cndmask_b32_e32 v147, v147, v148, vcc
	v_mul_f32_e32 v148, 0x3c800000, v147
	v_pk_mul_f32 v[64:65], v[64:65], v[148:149] op_sel_hi:[1,0]
	v_pk_mul_f32 v[62:63], v[62:63], v[148:149] op_sel_hi:[1,0]
	v_pk_mul_f32 v[60:61], v[60:61], v[148:149] op_sel_hi:[1,0]
	s_and_b64 vcc, exec, s[10:11]
	v_pk_mul_f32 v[58:59], v[58:59], v[148:149] op_sel_hi:[1,0]
	s_cbranch_vccnz .LBB0_780
	s_cmp_lt_i32 s3, 2
	s_cbranch_scc1 .LBB0_776
	s_cmp_lg_u32 s3, 2
	s_cselect_b64 s[52:53], -1, 0
	s_cbranch_execz .LBB0_777
	s_branch .LBB0_778
